# scan+topk phase: waves 4-7 run topk first then the scan (waves 0-3 unchanged) so each SIMD pairs a memory-streaming wave with a computing wave
# speedup vs baseline: 1.0100x; 1.0100x over previous
.LBB0_501:
	s_andn2_b64 vcc, exec, s[0:1]
	s_cbranch_vccnz .LBB0_1229
	s_mov_b32 s2, 0
	s_nop 0
	v_writelane_b32 v255, s2, 50
.Lk2_again:
	s_waitcnt vmcnt(15)
	v_mbcnt_lo_u32_b32 v0, -1, 0
	v_mbcnt_hi_u32_b32 v0, -1, v0
	v_readlane_b32 s0, v253, 8
	v_add_u32_e32 v91, s95, v0
	s_nop 0
	v_add_u32_e32 v99, s0, v91
	v_readlane_b32 s0, v251, 10
	v_readlane_b32 s1, v251, 11
	v_readlane_b32 s2, v251, 12
	v_readlane_b32 s3, v251, 13
	s_mov_b64 s[0:1], s[2:3]
	s_mov_b32 s2, 0x20000
	v_readfirstlane_b32 s10, v91
	v_cmp_gt_i32_e32 vcc, s2, v99
	v_readlane_b32 s4, v255, 50
	s_cmp_lg_u32 s4, 0
	s_cbranch_scc1 .Lk2_scan
	s_bitcmp1_b32 s10, 8
	s_cbranch_scc0 .Lk2_scan
	s_mov_b32 s4, 1
	s_nop 0
	v_writelane_b32 v255, s4, 50
	s_branch .Lk2_topk
.Lk2_scan:
	s_and_saveexec_b64 s[2:3], vcc
	s_mov_b32 s12, 0x800000
	s_cbranch_execz .LBB0_505
	s_add_u32 s4, s0, 0x40e00000
	s_addc_u32 s5, s1, 0
	s_add_u32 s6, s0, 0x41200000
	v_and_b32_e32 v0, 15, v91
	v_readlane_b32 s8, v253, 62
	s_addc_u32 s7, s1, 0
	v_lshlrev_b32_e32 v74, 4, v0
	v_lshl_add_u32 v103, v91, 3, s8
	s_mov_b64 s[8:9], 0

.LBB0_505:
	s_or_b64 exec, exec, s[2:3]
	v_readlane_b32 s2, v255, 50
	s_cmp_eq_u32 s2, 2
	s_cbranch_scc1 .Lk2_done
.Lk2_topk:
	s_ashr_i32 s2, s10, 6
	v_readlane_b32 s3, v253, 6
	s_add_i32 s4, s2, s3
	s_cmpk_gt_i32 s4, 0x1fff
	s_cbranch_scc1 .LBB0_1175
	s_mulk_i32 s2, 0x2600
	v_and_b32_e32 v0, 63, v91
	s_add_i32 s86, s2, 0
	s_sub_i32 s2, 0xfff, s4
	v_writelane_b32 v254, s2, 15
	v_cmp_eq_u32_e64 s[2:3], 63, v0
	s_waitcnt vmcnt(14)
	v_lshlrev_b32_e32 v7, 2, v0
	v_add_u32_e32 v32, 4, v7
	v_writelane_b32 v254, s2, 16
	v_and_b32_e32 v85, 0xfc, v32
	v_add_u32_e32 v32, 8, v7
	v_writelane_b32 v254, s3, 17
	v_cmp_gt_u32_e64 s[2:3], 62, v0
	v_and_b32_e32 v86, 0xfc, v32
	v_add_u32_e32 v32, 16, v7
	v_writelane_b32 v254, s2, 18
	v_lshlrev_b64 v[2:3], v91, -1
	v_and_b32_e32 v87, 0xfc, v32
	v_writelane_b32 v254, s3, 19
	v_cmp_gt_u32_e64 s[2:3], 60, v0
	v_add_u32_e32 v32, 32, v7
	v_not_b32_e32 v1, v3
	v_writelane_b32 v254, s2, 20
	s_waitcnt vmcnt(10)
	v_add_u32_e32 v21, s86, v7
	v_mul_u32_u24_e32 v3, 12, v0
	v_writelane_b32 v254, s3, 21
	v_cmp_gt_u32_e64 s[2:3], 56, v0
	s_waitcnt lgkmcnt(0)
	v_lshlrev_b32_e32 v5, 3, v0
	v_and_b32_e32 v88, 0xfc, v32
	v_writelane_b32 v254, s2, 22
	v_add_u32_e32 v32, 64, v7
	v_not_b32_e32 v2, v2
	v_writelane_b32 v254, s3, 23
	v_cmp_gt_u32_e64 s[2:3], 48, v0
	v_xor_b32_e32 v9, 4, v7
	v_xor_b32_e32 v11, 8, v7
	v_writelane_b32 v254, s2, 24
	v_xor_b32_e32 v13, 16, v7
	v_xor_b32_e32 v15, 32, v7
	v_writelane_b32 v254, s3, 25
	v_cmp_gt_u32_e64 s[2:3], 32, v0
	v_xor_b32_e32 v17, 64, v7
	v_xor_b32_e32 v19, 0x80, v7
	v_writelane_b32 v254, s2, 26
	v_or_b32_e32 v23, 64, v0
	s_waitcnt vmcnt(9)
	v_or_b32_e32 v25, 1, v7
	v_writelane_b32 v254, s3, 27
	s_add_u32 s2, s0, 0x55200000
	v_writelane_b32 v254, s2, 28
	s_addc_u32 s2, s1, 0
	v_writelane_b32 v254, s2, 29
	s_add_u32 s0, s0, 0x5d200000
	v_writelane_b32 v254, s0, 30
	s_addc_u32 s0, s1, 0
	v_writelane_b32 v254, s0, 31
	s_add_i32 s0, s86, 0x600
	v_writelane_b32 v254, s0, 32
	v_or_b32_e32 v27, 2, v7
	s_waitcnt vmcnt(8)
	v_or_b32_e32 v29, 3, v7
	v_or_b32_e32 v31, 0x100, v0
	s_waitcnt vmcnt(7)
	v_or_b32_e32 v39, 0x140, v0
	v_or_b32_e32 v41, 0x180, v0
	s_waitcnt vmcnt(6)
	v_or_b32_e32 v43, 0x1c0, v0
	v_or_b32_e32 v45, 0x200, v0
	s_waitcnt vmcnt(5)
	v_or_b32_e32 v47, 0x240, v0
	v_or_b32_e32 v49, 0x280, v0
	s_waitcnt vmcnt(4)
	v_or_b32_e32 v51, 0x2c0, v0
	v_or_b32_e32 v53, 0x300, v0
	s_waitcnt vmcnt(3)
	v_or_b32_e32 v55, 0x340, v0
	v_or_b32_e32 v57, 0x380, v0
	s_waitcnt vmcnt(2)
	v_or_b32_e32 v59, 0x3c0, v0
	v_or_b32_e32 v61, 0x400, v0
	s_waitcnt vmcnt(1)
	v_or_b32_e32 v63, 0x440, v0
	v_or_b32_e32 v65, 0x480, v0
	s_waitcnt vmcnt(0)
	v_or_b32_e32 v67, 0x4c0, v0
	v_or_b32_e32 v69, 0x500, v0
	v_or_b32_e32 v71, 0x540, v0
	v_or_b32_e32 v73, 0x580, v0
	v_or_b32_e32 v76, 0x5c0, v0
	v_or_b32_e32 v77, 0x600, v0
	v_or_b32_e32 v78, 0x640, v0
	v_or_b32_e32 v79, 0x680, v0
	v_or_b32_e32 v80, 0x6c0, v0
	v_or_b32_e32 v81, 0x700, v0
	v_or_b32_e32 v82, 0x740, v0
	v_or_b32_e32 v83, 0x780, v0
	v_or_b32_e32 v84, 0x7c0, v0
	v_or_b32_e32 v4, 0x800, v0
	v_or_b32_e32 v6, 0x840, v0
	v_or_b32_e32 v8, 0x880, v0
	v_or_b32_e32 v10, 0x8c0, v0
	v_or_b32_e32 v12, 0x900, v0
	v_or_b32_e32 v14, 0x940, v0
	v_or_b32_e32 v16, 0x980, v0
	v_or_b32_e32 v18, 0x9c0, v0
	v_or_b32_e32 v20, 0xa00, v0
	v_or_b32_e32 v22, 0xa40, v0
	v_or_b32_e32 v24, 0xa80, v0
	v_or_b32_e32 v26, 0xac0, v0
	v_or_b32_e32 v28, 0xb00, v0
	v_or_b32_e32 v30, 0xb40, v0
	v_or_b32_e32 v38, 0xb80, v0
	v_or_b32_e32 v40, 0xbc0, v0
	v_or_b32_e32 v42, 0xc00, v0
	v_or_b32_e32 v44, 0xc40, v0
	v_or_b32_e32 v46, 0xc80, v0
	v_or_b32_e32 v48, 0xcc0, v0
	v_or_b32_e32 v50, 0xd00, v0
	v_or_b32_e32 v52, 0xd40, v0
	v_or_b32_e32 v54, 0xd80, v0
	v_or_b32_e32 v56, 0xdc0, v0
	v_or_b32_e32 v58, 0xe00, v0
	v_or_b32_e32 v60, 0xe40, v0
	v_or_b32_e32 v62, 0xe80, v0
	v_or_b32_e32 v64, 0xec0, v0
	v_or_b32_e32 v66, 0xf00, v0
	v_or_b32_e32 v68, 0xf40, v0
	v_or_b32_e32 v70, 0xf80, v0
	v_or_b32_e32 v72, 0xfc0, v0
	v_cmp_eq_u32_e64 s[36:37], 0, v0
	v_and_b32_e32 v89, 0xfc, v32
	v_or_b32_e32 v90, 0x80, v0
	v_or_b32_e32 v91, 0xc0, v0
	v_add_u32_e32 v92, v21, v3
	v_add_u32_e32 v93, s86, v5
	s_mov_b32 s2, s4
	v_writelane_b32 v254, s4, 33
	s_branch .LBB0_509

.LBB0_1175:
	v_readlane_b32 s0, v255, 50
	s_cmp_eq_u32 s0, 1
	s_cbranch_scc0 .Lk2_done
	s_mov_b32 s0, 2
	s_nop 0
	v_writelane_b32 v255, s0, 50
	s_branch .Lk2_again
